# row-tile table build before the expert GEMMs: DPP wave prefix scan + batched LDS reads with compare/add-carry instead of two serial LDS loops
# speedup vs baseline: 1.0067x; 1.0067x over previous
.LBB0_1842:
	s_or_b64 exec, exec, s[4:5]
	v_cmp_gt_u32_e32 vcc, 33, v0
	s_waitcnt lgkmcnt(0)
	s_barrier
	s_and_saveexec_b64 s[4:5], vcc
	s_cbranch_execz .LBB0_1866
	s_mov_b64 s[6:7], exec
	s_mov_b64 exec, -1
	s_mov_b32 s2, 0x201c0
	v_lshl_add_u32 v2, v0, 2, s2
	ds_read_b32 v3, v2
	v_cmp_gt_u32_e32 vcc, 32, v0
	s_waitcnt lgkmcnt(0)
	v_add_u32_e32 v3, 0xff, v3
	v_ashrrev_i32_e32 v3, 8, v3
	v_cndmask_b32_e32 v3, 0, v3, vcc
	v_mov_b32_e32 v1, v3
	s_nop 1
	v_add_u32_dpp v1, v1, v1 row_shr:1 row_mask:0xf bank_mask:0xf bound_ctrl:0
	s_nop 1
	v_add_u32_dpp v1, v1, v1 row_shr:2 row_mask:0xf bank_mask:0xf bound_ctrl:0
	s_nop 1
	v_add_u32_dpp v1, v1, v1 row_shr:4 row_mask:0xf bank_mask:0xf bound_ctrl:0
	s_nop 1
	v_add_u32_dpp v1, v1, v1 row_shr:8 row_mask:0xf bank_mask:0xf bound_ctrl:0
	s_nop 1
	v_add_u32_dpp v1, v1, v1 row_bcast:15 row_mask:0xa bank_mask:0xf
	s_nop 1
	v_add_u32_dpp v1, v1, v1 row_bcast:31 row_mask:0xc bank_mask:0xf
	s_nop 1
	v_sub_u32_e32 v1, v1, v3
	s_mov_b64 exec, s[6:7]
	s_add_i32 s2, 0, 0x201c0
	s_waitcnt vmcnt(0)
	v_lshl_add_u32 v2, v0, 2, s2
	ds_write_b32 v2, v1 offset:128
.LBB0_1866:
	s_or_b64 exec, exec, s[4:5]
	s_movk_i32 s2, 0x120
	v_cmp_gt_u32_e32 vcc, s2, v0
	s_waitcnt lgkmcnt(0)
	s_barrier
	s_and_saveexec_b64 s[4:5], vcc
	s_cbranch_execz .LBB0_1879
	s_add_i32 s2, 0, 0x202c0
	v_mov_b32_e32 v1, s2
	ds_read_b32 v1, v1
	s_mov_b32 s2, 0
	s_waitcnt lgkmcnt(0)
	v_cmp_lt_i32_e32 vcc, v0, v1
	s_and_b64 exec, exec, vcc
	s_cbranch_execz .LBB0_1879
	s_waitcnt vmcnt(0)
	s_mov_b32 s2, 0x20240
	v_mov_b32_e32 v2, s2
	ds_read_b128 v[162:165], v2
	ds_read_b128 v[166:169], v2 offset:16
	ds_read_b128 v[170:173], v2 offset:32
	ds_read_b128 v[174:177], v2 offset:48
	ds_read_b128 v[178:181], v2 offset:64
	ds_read_b128 v[182:185], v2 offset:80
	ds_read_b128 v[186:189], v2 offset:96
	ds_read_b128 v[190:193], v2 offset:112
	v_mov_b32_e32 v1, 0
	s_waitcnt lgkmcnt(0)
	v_cmp_le_i32_e32 vcc, v163, v0
	v_addc_co_u32_e32 v1, vcc, 0, v1, vcc
	v_cmp_le_i32_e32 vcc, v164, v0
	v_addc_co_u32_e32 v1, vcc, 0, v1, vcc
	v_cmp_le_i32_e32 vcc, v165, v0
	v_addc_co_u32_e32 v1, vcc, 0, v1, vcc
	v_cmp_le_i32_e32 vcc, v166, v0
	v_addc_co_u32_e32 v1, vcc, 0, v1, vcc
	v_cmp_le_i32_e32 vcc, v167, v0
	v_addc_co_u32_e32 v1, vcc, 0, v1, vcc
	v_cmp_le_i32_e32 vcc, v168, v0
	v_addc_co_u32_e32 v1, vcc, 0, v1, vcc
	v_cmp_le_i32_e32 vcc, v169, v0
	v_addc_co_u32_e32 v1, vcc, 0, v1, vcc
	v_cmp_le_i32_e32 vcc, v170, v0
	v_addc_co_u32_e32 v1, vcc, 0, v1, vcc
	v_cmp_le_i32_e32 vcc, v171, v0
	v_addc_co_u32_e32 v1, vcc, 0, v1, vcc
	v_cmp_le_i32_e32 vcc, v172, v0
	v_addc_co_u32_e32 v1, vcc, 0, v1, vcc
	v_cmp_le_i32_e32 vcc, v173, v0
	v_addc_co_u32_e32 v1, vcc, 0, v1, vcc
	v_cmp_le_i32_e32 vcc, v174, v0
	v_addc_co_u32_e32 v1, vcc, 0, v1, vcc
	v_cmp_le_i32_e32 vcc, v175, v0
	v_addc_co_u32_e32 v1, vcc, 0, v1, vcc
	v_cmp_le_i32_e32 vcc, v176, v0
	v_addc_co_u32_e32 v1, vcc, 0, v1, vcc
	v_cmp_le_i32_e32 vcc, v177, v0
	v_addc_co_u32_e32 v1, vcc, 0, v1, vcc
	v_cmp_le_i32_e32 vcc, v178, v0
	v_addc_co_u32_e32 v1, vcc, 0, v1, vcc
	v_cmp_le_i32_e32 vcc, v179, v0
	v_addc_co_u32_e32 v1, vcc, 0, v1, vcc
	v_cmp_le_i32_e32 vcc, v180, v0
	v_addc_co_u32_e32 v1, vcc, 0, v1, vcc
	v_cmp_le_i32_e32 vcc, v181, v0
	v_addc_co_u32_e32 v1, vcc, 0, v1, vcc
	v_cmp_le_i32_e32 vcc, v182, v0
	v_addc_co_u32_e32 v1, vcc, 0, v1, vcc
	v_cmp_le_i32_e32 vcc, v183, v0
	v_addc_co_u32_e32 v1, vcc, 0, v1, vcc
	v_cmp_le_i32_e32 vcc, v184, v0
	v_addc_co_u32_e32 v1, vcc, 0, v1, vcc
	v_cmp_le_i32_e32 vcc, v185, v0
	v_addc_co_u32_e32 v1, vcc, 0, v1, vcc
	v_cmp_le_i32_e32 vcc, v186, v0
	v_addc_co_u32_e32 v1, vcc, 0, v1, vcc
	v_cmp_le_i32_e32 vcc, v187, v0
	v_addc_co_u32_e32 v1, vcc, 0, v1, vcc
	v_cmp_le_i32_e32 vcc, v188, v0
	v_addc_co_u32_e32 v1, vcc, 0, v1, vcc
	v_cmp_le_i32_e32 vcc, v189, v0
	v_addc_co_u32_e32 v1, vcc, 0, v1, vcc
	v_cmp_le_i32_e32 vcc, v190, v0
	v_addc_co_u32_e32 v1, vcc, 0, v1, vcc
	v_cmp_le_i32_e32 vcc, v191, v0
	v_addc_co_u32_e32 v1, vcc, 0, v1, vcc
	v_cmp_le_i32_e32 vcc, v192, v0
	v_addc_co_u32_e32 v1, vcc, 0, v1, vcc
	v_cmp_le_i32_e32 vcc, v193, v0
	v_addc_co_u32_e32 v1, vcc, 0, v1, vcc
	v_mov_b32_e32 v3, 0
	v_cmp_ne_u32_e32 vcc, 0, v1
	s_and_saveexec_b64 s[6:7], vcc
	s_cbranch_execz .LBB0_1878
	s_add_i32 s2, 0, 0x20240
	v_lshl_add_u32 v2, v1, 2, s2
	s_mov_b64 s[8:9], 0
	s_branch .LBB0_1875
